# baseline (speedup 1.0000x reference)
_Z10kvq_kernelPKtS0_PtS1_S1_PKf:
	s_ashr_i32 s3, s2, 31
	s_lshr_b32 s3, s3, 29
	s_add_i32 s3, s2, s3
	v_lshlrev_b32_e32 v1, 4, v0
	v_and_b32_e32 v2, 32, v0
	s_ashr_i32 s3, s3, 3
	v_bitop3_b32 v1, v1, v2, 48 bitop3:0x6c
	v_lshrrev_b32_e32 v2, 1, v0
	v_lshrrev_b32_e32 v4, 5, v0
	s_lshl_b32 s2, s2, 5
	s_mul_i32 s12, s3, 0xffffff01
	v_and_b32_e32 v2, 24, v2
	v_and_b32_e32 v4, 4, v4
	v_bfe_u32 v5, v0, 2, 2
	s_add_i32 s12, s12, s2
	v_bfe_u32 v3, v0, 2, 4
	v_or3_b32 v2, v4, v5, v2
	v_lshrrev_b32_e32 v4, 3, v0
	s_load_dwordx8 s[4:11], s[0:1], 0x0
	s_ashr_i32 s2, s12, 5
	s_and_b32 s13, s3, 7
	s_lshr_b32 s3, s3, 3
	v_and_or_b32 v1, v0, 64, v1
	v_and_or_b32 v5, v4, 48, v3
	v_and_or_b32 v4, v4, 32, v2
	s_lshl_b32 s12, s2, 3
	s_add_i32 s2, s2, s3
	v_lshl_or_b32 v84, v4, 11, v1
	v_bfe_u32 v4, v0, 3, 25
	s_or_b32 s14, s12, s13
	s_and_b32 s23, s2, 3
	v_or_b32_e32 v4, 64, v4
	s_movk_i32 s2, 0x70
	v_readfirstlane_b32 s18, v0
	v_and_or_b32 v3, v4, s2, v3
	s_movk_i32 s2, 0x60
	s_ashr_i32 s15, s14, 31
	s_lshr_b32 s16, s18, 8
	v_and_or_b32 v2, v4, s2, v2
	s_lshl_b64 s[2:3], s[14:15], 18
	s_waitcnt lgkmcnt(0)
	s_add_u32 s4, s4, s2
	s_addc_u32 s5, s5, s3
	s_lshr_b32 s2, s18, 1
	s_lshl_b32 s3, s18, 4
	s_and_b32 s3, s3, 0xfffffc00
	s_and_b32 s15, s2, 0x60
	s_lshl_b32 s2, s23, 19
	s_add_u32 s12, s6, s2
	s_addc_u32 s13, s7, 0
	s_add_i32 s19, s3, 0
	s_add_i32 m0, s19, 0x4000
	v_lshl_or_b32 v88, v2, 11, v1
	v_add_u32_e32 v172, 0x40000, v84
	v_add_u32_e32 v173, 0x40000, v88
	global_load_lds_dwordx4 v84, s[12:13]
	s_add_i32 m0, s19, 0x6000
	v_lshl_or_b32 v82, v5, 11, v1
	global_load_lds_dwordx4 v88, s[12:13]
	s_mov_b32 m0, s19
	s_add_u32 s2, s12, 0x40000
	v_mov_b32_e32 v2, 0
	global_load_lds_dwordx4 v82, s[4:5]
	s_addc_u32 s3, s13, 0
	s_add_i32 m0, s19, 0x8000
	v_mov_b32_e32 v85, v2
	global_load_lds_dwordx4 v84, s[2:3]
	s_add_i32 m0, s19, 0xa000
	v_lshl_or_b32 v86, v3, 11, v1
	v_lshl_add_u64 v[4:5], s[12:13], 0, v[84:85]
	v_mov_b32_e32 v89, v2
	global_load_lds_dwordx4 v88, s[2:3]
	s_add_i32 m0, s19, 0x2000
	s_mov_b64 s[2:3], 0x80
	v_lshl_add_u64 v[6:7], s[12:13], 0, v[88:89]
	global_load_lds_dwordx4 v86, s[4:5]
	v_lshl_add_u64 v[4:5], v[4:5], 0, s[2:3]
	s_add_i32 m0, s19, 0x10000
	v_mov_b32_e32 v83, v2
	global_load_lds_dwordx4 v[4:5], off
	v_lshl_add_u64 v[4:5], v[6:7], 0, s[2:3]
	s_add_i32 m0, s19, 0x12000
	v_lshl_add_u64 v[8:9], s[4:5], 0, v[82:83]
	global_load_lds_dwordx4 v[4:5], off
	s_add_i32 m0, s19, 0xc000
	v_lshl_add_u64 v[4:5], v[8:9], 0, s[2:3]
	s_add_u32 s20, s12, 0x40080
	v_mov_b32_e32 v87, v2
	global_load_lds_dwordx4 v[4:5], off
	s_addc_u32 s21, s13, 0
	s_add_i32 m0, s19, 0x14000
	v_lshl_add_u64 v[10:11], s[4:5], 0, v[86:87]
	global_load_lds_dwordx4 v84, s[20:21]
	s_add_i32 m0, s19, 0x16000
	v_lshl_add_u64 v[4:5], v[10:11], 0, s[2:3]
	global_load_lds_dwordx4 v88, s[20:21]
	s_add_i32 m0, s19, 0xe000
	s_load_dwordx4 s[0:3], s[0:1], 0x20
	global_load_lds_dwordx4 v[4:5], off
	s_lshl_b32 s20, s23, 10
	v_bfe_u32 v3, v0, 4, 2
	s_waitcnt lgkmcnt(0)
	s_add_u32 s20, s2, s20
	s_addc_u32 s21, s3, 0
	s_lshl_b32 s22, s15, 2
	s_add_u32 s26, s20, s22
	s_addc_u32 s27, s21, 0
	v_lshlrev_b32_e32 v4, 5, v3
	v_mov_b32_e32 v5, v2
	v_lshl_add_u64 v[4:5], s[26:27], 0, v[4:5]
	global_load_dwordx4 v[18:21], v[4:5], off
	global_load_dwordx4 v[14:17], v[4:5], off offset:16
	global_load_dwordx4 v[10:13], v[4:5], off offset:512
	global_load_dwordx4 v[6:9], v[4:5], off offset:528
	s_waitcnt vmcnt(6)
	v_lshlrev_b32_e32 v1, 3, v3
	s_mov_b32 s17, 0
	s_mov_b32 s24, 0xc000
	s_mov_b32 s3, 2
	s_cmp_lg_u32 s16, 1
	s_cbranch_scc1 .LBB1_2
	s_barrier
.LBB1_2:
	v_and_b32_e32 v93, 15, v0
	v_lshlrev_b32_e32 v100, 4, v3
	v_lshlrev_b32_e32 v3, 6, v0
	s_movk_i32 s26, 0x3c0
	v_lshrrev_b32_e32 v92, 4, v0
	s_lshl_b32 s2, s23, 8
	s_lshl_b32 s25, s16, 6
	v_lshl_or_b32 v90, v93, 6, v100
	v_and_or_b32 v3, v3, s26, v100
	v_lshlrev_b32_e32 v0, 2, v0
	s_lshl_b32 s16, s16, 13
	s_lshl_b32 s26, s15, 7
	v_and_b32_e32 v0, 32, v0
	s_barrier
	s_add_i32 s16, s16, 0
	s_add_i32 s26, s26, 0
	v_xad_u32 v91, v90, v0, s16
	v_xad_u32 v101, v3, v0, s26
	s_mov_b32 s27, 0x18000
	s_mov_b32 s26, 15
	s_mov_b32 s28, 0
	s_mov_b32 s16, 0
	v_mov_b32_e32 v3, v2
	v_mov_b32_e32 v4, v2
	v_mov_b32_e32 v5, v2
	v_mov_b32_e32 v22, v2
	v_mov_b32_e32 v23, v2
	v_mov_b32_e32 v24, v2
	v_mov_b32_e32 v25, v2
	v_mov_b32_e32 v30, v2
	v_mov_b32_e32 v31, v2
	v_mov_b32_e32 v32, v2
	v_mov_b32_e32 v33, v2
	v_mov_b32_e32 v38, v2
	v_mov_b32_e32 v39, v2
	v_mov_b32_e32 v40, v2
	v_mov_b32_e32 v41, v2
	v_mov_b32_e32 v42, v2
	v_mov_b32_e32 v43, v2
	v_mov_b32_e32 v44, v2
	v_mov_b32_e32 v45, v2
	v_mov_b32_e32 v50, v2
	v_mov_b32_e32 v51, v2
	v_mov_b32_e32 v52, v2
	v_mov_b32_e32 v53, v2
	v_mov_b32_e32 v62, v2
	v_mov_b32_e32 v63, v2
	v_mov_b32_e32 v64, v2
	v_mov_b32_e32 v65, v2
	v_mov_b32_e32 v70, v2
	v_mov_b32_e32 v71, v2
	v_mov_b32_e32 v72, v2
	v_mov_b32_e32 v73, v2
	v_mov_b32_e32 v26, v2
	v_mov_b32_e32 v27, v2
	v_mov_b32_e32 v28, v2
	v_mov_b32_e32 v29, v2
	v_mov_b32_e32 v34, v2
	v_mov_b32_e32 v35, v2
	v_mov_b32_e32 v36, v2
	v_mov_b32_e32 v37, v2
	v_mov_b32_e32 v46, v2
	v_mov_b32_e32 v47, v2
	v_mov_b32_e32 v48, v2
	v_mov_b32_e32 v49, v2
	v_mov_b32_e32 v54, v2
	v_mov_b32_e32 v55, v2
	v_mov_b32_e32 v56, v2
	v_mov_b32_e32 v57, v2
	v_mov_b32_e32 v58, v2
	v_mov_b32_e32 v59, v2
	v_mov_b32_e32 v60, v2
	v_mov_b32_e32 v61, v2
	v_mov_b32_e32 v66, v2
	v_mov_b32_e32 v67, v2
	v_mov_b32_e32 v68, v2
	v_mov_b32_e32 v69, v2
	v_mov_b32_e32 v74, v2
	v_mov_b32_e32 v75, v2
	v_mov_b32_e32 v76, v2
	v_mov_b32_e32 v77, v2
	v_mov_b32_e32 v78, v2
	v_mov_b32_e32 v79, v2
	v_mov_b32_e32 v80, v2
	v_mov_b32_e32 v81, v2
.LBB1_3:
	s_mov_b32 s29, s16
	v_add_u32_e32 v0, s29, v101
	ds_read_b128 v[94:97], v0 offset:16384
	ds_read_b128 v[102:105], v0 offset:17408
	ds_read_b128 v[106:109], v0 offset:18432
	ds_read_b128 v[110:113], v0 offset:19456
	ds_read_b128 v[114:117], v0 offset:32768
	ds_read_b128 v[118:121], v0 offset:33792
	ds_read_b128 v[122:125], v0 offset:34816
	ds_read_b128 v[126:129], v0 offset:35840
	v_add_u32_e32 v0, s29, v91
	ds_read_b128 v[130:133], v0
	ds_read_b128 v[134:137], v0 offset:1024
	ds_read_b128 v[138:141], v0 offset:2048
	ds_read_b128 v[142:145], v0 offset:3072
	ds_read_b128 v[146:149], v0 offset:4096
	ds_read_b128 v[150:153], v0 offset:5120
	ds_read_b128 v[154:157], v0 offset:6144
	ds_read_b128 v[158:161], v0 offset:7168
	s_lshl_b32 s16, s28, 2
	s_or_b32 s16, s16, s23
	s_lshl_b64 s[30:31], s[16:17], 19
	s_add_u32 s16, s6, s30
	s_addc_u32 s31, s7, s31
	s_lshl_b32 s33, s3, 7
	s_ashr_i32 s35, s33, 31
	s_add_u32 s30, s16, s33
	s_addc_u32 s31, s31, s35
	s_add_u32 s34, s4, s33
	s_addc_u32 s35, s5, s35
	s_add_i32 s16, s19, s27
	s_add_i32 m0, s16, 0x4000
	s_nop 0
	global_load_lds_dwordx4 v84, s[30:31]
	s_add_i32 m0, s16, 0x6000
	s_nop 0
	global_load_lds_dwordx4 v88, s[30:31]
	s_mov_b32 m0, s16
	s_nop 0
	global_load_lds_dwordx4 v82, s[34:35]
	s_waitcnt vmcnt(3)
	s_waitcnt lgkmcnt(0)
	s_barrier
	s_setprio 1
	s_waitcnt lgkmcnt(0)
	v_mfma_f32_16x16x32_f16 v[78:81], v[94:97], v[130:133], v[78:81]
	s_add_i32 m0, s16, 0x8000
	v_mfma_f32_16x16x32_f16 v[74:77], v[106:109], v[130:133], v[74:77]
	global_load_lds_dwordx4 v172, s[30:31]
	s_add_i32 m0, s16, 0xa000
	v_mfma_f32_16x16x32_f16 v[66:69], v[94:97], v[138:141], v[66:69]
	global_load_lds_dwordx4 v173, s[30:31]
	s_add_i32 m0, s16, 0x2000
	v_mfma_f32_16x16x32_f16 v[58:61], v[106:109], v[138:141], v[58:61]
	global_load_lds_dwordx4 v86, s[34:35]
	v_mfma_f32_16x16x32_f16 v[78:81], v[102:105], v[134:137], v[78:81]
	v_mfma_f32_16x16x32_f16 v[74:77], v[110:113], v[134:137], v[74:77]
	v_mfma_f32_16x16x32_f16 v[66:69], v[102:105], v[142:145], v[66:69]
	v_mfma_f32_16x16x32_f16 v[58:61], v[110:113], v[142:145], v[58:61]
	v_mfma_f32_16x16x32_f16 v[54:57], v[94:97], v[146:149], v[54:57]
	v_mfma_f32_16x16x32_f16 v[46:49], v[106:109], v[146:149], v[46:49]
	v_mfma_f32_16x16x32_f16 v[34:37], v[94:97], v[154:157], v[34:37]
	v_mfma_f32_16x16x32_f16 v[26:29], v[106:109], v[154:157], v[26:29]
	v_mfma_f32_16x16x32_f16 v[54:57], v[102:105], v[150:153], v[54:57]
	v_mfma_f32_16x16x32_f16 v[46:49], v[110:113], v[150:153], v[46:49]
	v_mfma_f32_16x16x32_f16 v[34:37], v[102:105], v[158:161], v[34:37]
	v_mfma_f32_16x16x32_f16 v[26:29], v[110:113], v[158:161], v[26:29]
	v_mfma_f32_16x16x32_f16 v[70:73], v[114:117], v[130:133], v[70:73]
	v_mfma_f32_16x16x32_f16 v[62:65], v[122:125], v[130:133], v[62:65]
	v_mfma_f32_16x16x32_f16 v[50:53], v[114:117], v[138:141], v[50:53]
	v_mfma_f32_16x16x32_f16 v[42:45], v[122:125], v[138:141], v[42:45]
	v_mfma_f32_16x16x32_f16 v[70:73], v[118:121], v[134:137], v[70:73]
	v_mfma_f32_16x16x32_f16 v[62:65], v[126:129], v[134:137], v[62:65]
	v_mfma_f32_16x16x32_f16 v[50:53], v[118:121], v[142:145], v[50:53]
	v_mfma_f32_16x16x32_f16 v[42:45], v[126:129], v[142:145], v[42:45]
	v_mfma_f32_16x16x32_f16 v[38:41], v[114:117], v[146:149], v[38:41]
	v_mfma_f32_16x16x32_f16 v[30:33], v[122:125], v[146:149], v[30:33]
	s_add_i32 s3, s3, 1
	s_bitcmp1_b32 s3, 4
	s_addc_u32 s28, s28, 0
	v_mfma_f32_16x16x32_f16 v[22:25], v[114:117], v[154:157], v[22:25]
	s_and_b32 s3, s3, 15
	v_mfma_f32_16x16x32_f16 v[2:5], v[122:125], v[154:157], v[2:5]
	v_mfma_f32_16x16x32_f16 v[38:41], v[118:121], v[150:153], v[38:41]
	v_mfma_f32_16x16x32_f16 v[30:33], v[126:129], v[150:153], v[30:33]
	v_mfma_f32_16x16x32_f16 v[22:25], v[118:121], v[158:161], v[22:25]
	s_mov_b32 s16, s24
	s_mov_b32 s24, s27
	v_mfma_f32_16x16x32_f16 v[2:5], v[126:129], v[158:161], v[2:5]
	s_mov_b32 s27, s29
	s_add_u32 s26, s26, -1
	s_setprio 0
	s_barrier
	s_cbranch_scc1 .LBB1_3
	s_lshl_b32 s3, s14, 7
	s_add_i32 s17, s25, s3
	s_ashr_i32 s3, s17, 1
	s_lshr_b32 s14, s17, 5
	s_or_b32 s24, s15, s2
	s_and_b32 s14, s14, 62
	s_and_b32 s27, s3, 0xfffffc00
	v_or_b32_e32 v105, s24, v1
	v_lshlrev_b32_e32 v98, 4, v93
	v_or_b32_e32 v102, 16, v93
	v_or_b32_e32 v103, 32, v93
	v_or_b32_e32 v104, 48, v93
	v_mov_b32_e32 v93, 0
	s_and_b32 s16, s24, 0x340
	v_lshlrev_b32_e32 v95, 6, v105
	s_or_b32 s2, s27, s14
	v_lshlrev_b32_e32 v0, 9, v92
	v_and_b32_e32 v110, 0xc00, v95
	v_mov_b32_e32 v111, v93
	s_or_b32 s14, s2, s16
	v_and_b32_e32 v92, 0x200, v0
	v_lshl_add_u64 v[110:111], s[8:9], 0, v[110:111]
	s_or_b32 s30, s14, 0x80
	s_mov_b32 s3, 0
	v_mov_b32_e32 v99, v93
	v_lshl_add_u64 v[110:111], v[110:111], 0, v[92:93]
	s_mov_b32 s2, 0x3e38aa3b
	v_pk_add_f32 v[72:73], v[12:13], v[72:73]
	v_pk_add_f32 v[70:71], v[10:11], v[70:71]
	v_pk_add_f32 v[64:65], v[8:9], v[64:65]
	v_pk_add_f32 v[62:63], v[6:7], v[62:63]
	s_ashr_i32 s31, s30, 31
	v_lshl_add_u64 v[112:113], v[110:111], 0, v[98:99]
	v_pk_mul_f32 v[72:73], v[72:73], s[2:3] op_sel_hi:[1,0]
	v_pk_mul_f32 v[70:71], v[70:71], s[2:3] op_sel_hi:[1,0]
	v_pk_mul_f32 v[64:65], v[64:65], s[2:3] op_sel_hi:[1,0]
	v_pk_mul_f32 v[62:63], v[62:63], s[2:3] op_sel_hi:[1,0]
	s_lshl_b64 s[30:31], s[30:31], 12
	v_lshlrev_b32_e32 v96, 4, v102
	v_mov_b32_e32 v97, v93
	v_pk_add_f32 v[80:81], v[20:21], v[80:81]
	v_pk_add_f32 v[78:79], v[18:19], v[78:79]
	v_pk_add_f32 v[74:75], v[14:15], v[74:75]
	s_ashr_i32 s15, s14, 31
	v_cvt_pk_f16_f32 v70, v70, v71
	v_cvt_pk_f16_f32 v71, v72, v73
	v_cvt_pk_f16_f32 v72, v62, v63
	v_cvt_pk_f16_f32 v73, v64, v65
	v_lshl_add_u64 v[62:63], v[112:113], 0, s[30:31]
	v_pk_add_f32 v[58:59], v[14:15], v[58:59]
	v_pk_mul_f32 v[80:81], v[80:81], s[2:3] op_sel_hi:[1,0]
	v_pk_mul_f32 v[78:79], v[78:79], s[2:3] op_sel_hi:[1,0]
	v_pk_mul_f32 v[74:75], v[74:75], s[2:3] op_sel_hi:[1,0]
	s_lshl_b64 s[28:29], s[14:15], 12
	global_store_dwordx4 v[62:63], v[70:73], off
	v_pk_add_f32 v[62:63], v[20:21], v[68:69]
	v_pk_add_f32 v[64:65], v[18:19], v[66:67]
	v_lshl_add_u64 v[70:71], v[110:111], 0, v[96:97]
	v_pk_mul_f32 v[58:59], v[58:59], s[2:3] op_sel_hi:[1,0]
	v_pk_add_f32 v[52:53], v[12:13], v[52:53]
	v_pk_add_f32 v[50:51], v[10:11], v[50:51]
	v_pk_add_f32 v[44:45], v[8:9], v[44:45]
	v_pk_add_f32 v[42:43], v[6:7], v[42:43]
	v_lshlrev_b32_e32 v0, 4, v103
	v_cvt_pk_f16_f32 v78, v78, v79
	v_cvt_pk_f16_f32 v79, v80, v81
	v_cvt_pk_f16_f32 v80, v74, v75
	v_lshl_add_u64 v[74:75], v[112:113], 0, s[28:29]
	v_pk_mul_f32 v[66:67], v[62:63], s[2:3] op_sel_hi:[1,0]
	v_pk_mul_f32 v[62:63], v[64:65], s[2:3] op_sel_hi:[1,0]
	v_cvt_pk_f16_f32 v64, v58, v59
	v_lshl_add_u64 v[58:59], v[70:71], 0, s[28:29]
	v_pk_mul_f32 v[52:53], v[52:53], s[2:3] op_sel_hi:[1,0]
	v_pk_mul_f32 v[50:51], v[50:51], s[2:3] op_sel_hi:[1,0]
	v_pk_mul_f32 v[44:45], v[44:45], s[2:3] op_sel_hi:[1,0]
	v_pk_mul_f32 v[42:43], v[42:43], s[2:3] op_sel_hi:[1,0]
	s_or_b32 s28, s14, 1
	s_or_b32 s14, s14, 0x81
	v_and_b32_e32 v106, 0xf0, v0
	v_mov_b32_e32 v107, v93
	v_cvt_pk_f16_f32 v50, v50, v51
	v_cvt_pk_f16_f32 v51, v52, v53
	v_cvt_pk_f16_f32 v52, v42, v43
	v_cvt_pk_f16_f32 v53, v44, v45
	v_lshl_add_u64 v[42:43], v[70:71], 0, s[30:31]
	v_pk_add_f32 v[40:41], v[12:13], v[40:41]
	v_pk_add_f32 v[38:39], v[10:11], v[38:39]
	v_pk_add_f32 v[32:33], v[8:9], v[32:33]
	v_pk_add_f32 v[30:31], v[6:7], v[30:31]
	s_ashr_i32 s15, s14, 31
	v_lshlrev_b32_e32 v94, 4, v104
	global_store_dwordx4 v[42:43], v[50:53], off
	v_pk_mul_f32 v[40:41], v[40:41], s[2:3] op_sel_hi:[1,0]
	v_pk_mul_f32 v[38:39], v[38:39], s[2:3] op_sel_hi:[1,0]
	v_lshl_add_u64 v[50:51], v[110:111], 0, v[106:107]
	v_pk_mul_f32 v[32:33], v[32:33], s[2:3] op_sel_hi:[1,0]
	v_pk_mul_f32 v[30:31], v[30:31], s[2:3] op_sel_hi:[1,0]
	s_lshl_b64 s[14:15], s[14:15], 12
	v_and_b32_e32 v108, 0x1f0, v94
	v_mov_b32_e32 v109, v93
	v_pk_add_f32 v[42:43], v[20:21], v[56:57]
	v_pk_add_f32 v[44:45], v[18:19], v[54:55]
	v_pk_add_f32 v[46:47], v[14:15], v[46:47]
	s_ashr_i32 s29, s28, 31
	v_cvt_pk_f16_f32 v38, v38, v39
	v_cvt_pk_f16_f32 v39, v40, v41
	v_cvt_pk_f16_f32 v40, v30, v31
	v_cvt_pk_f16_f32 v41, v32, v33
	v_lshl_add_u64 v[30:31], v[50:51], 0, s[14:15]
	v_pk_add_f32 v[20:21], v[20:21], v[36:37]
	v_pk_add_f32 v[18:19], v[18:19], v[34:35]
	v_pk_add_f32 v[14:15], v[14:15], v[26:27]
	v_pk_add_f32 v[76:77], v[16:17], v[76:77]
	v_pk_add_f32 v[60:61], v[16:17], v[60:61]
	v_pk_mul_f32 v[52:53], v[42:43], s[2:3] op_sel_hi:[1,0]
	v_pk_mul_f32 v[42:43], v[44:45], s[2:3] op_sel_hi:[1,0]
	v_pk_add_f32 v[44:45], v[16:17], v[48:49]
	s_lshl_b64 s[28:29], s[28:29], 12
	global_store_dwordx4 v[30:31], v[38:41], off
	v_lshl_add_u64 v[30:31], v[110:111], 0, v[108:109]
	v_pk_mul_f32 v[20:21], v[20:21], s[2:3] op_sel_hi:[1,0]
	v_pk_mul_f32 v[18:19], v[18:19], s[2:3] op_sel_hi:[1,0]
	v_pk_add_f32 v[16:17], v[16:17], v[28:29]
	v_pk_mul_f32 v[14:15], v[14:15], s[2:3] op_sel_hi:[1,0]
	v_pk_add_f32 v[12:13], v[12:13], v[24:25]
	v_pk_add_f32 v[10:11], v[10:11], v[22:23]
	v_pk_add_f32 v[4:5], v[8:9], v[4:5]
	v_pk_add_f32 v[2:3], v[6:7], v[2:3]
	v_pk_mul_f32 v[76:77], v[76:77], s[2:3] op_sel_hi:[1,0]
	v_pk_mul_f32 v[60:61], v[60:61], s[2:3] op_sel_hi:[1,0]
	v_pk_mul_f32 v[48:49], v[44:45], s[2:3] op_sel_hi:[1,0]
	v_pk_mul_f32 v[44:45], v[46:47], s[2:3] op_sel_hi:[1,0]
	v_lshl_add_u64 v[46:47], v[50:51], 0, s[28:29]
	v_cvt_pk_f16_f32 v18, v18, v19
	v_cvt_pk_f16_f32 v19, v20, v21
	v_pk_mul_f32 v[16:17], v[16:17], s[2:3] op_sel_hi:[1,0]
	v_cvt_pk_f16_f32 v20, v14, v15
	v_lshl_add_u64 v[14:15], v[30:31], 0, s[28:29]
	v_pk_mul_f32 v[12:13], v[12:13], s[2:3] op_sel_hi:[1,0]
	v_pk_mul_f32 v[10:11], v[10:11], s[2:3] op_sel_hi:[1,0]
	v_pk_mul_f32 v[4:5], v[4:5], s[2:3] op_sel_hi:[1,0]
	v_pk_mul_f32 v[2:3], v[2:3], s[2:3] op_sel_hi:[1,0]
	s_add_u32 s28, s20, s22
	v_cvt_pk_f16_f32 v81, v76, v77
	v_cvt_pk_f16_f32 v62, v62, v63
	v_cvt_pk_f16_f32 v63, v66, v67
	v_cvt_pk_f16_f32 v65, v60, v61
	v_cvt_pk_f16_f32 v42, v42, v43
	v_cvt_pk_f16_f32 v43, v52, v53
	v_cvt_pk_f16_f32 v44, v44, v45
	v_cvt_pk_f16_f32 v45, v48, v49
	v_cvt_pk_f16_f32 v21, v16, v17
	v_cvt_pk_f16_f32 v10, v10, v11
	v_cvt_pk_f16_f32 v11, v12, v13
	v_cvt_pk_f16_f32 v12, v2, v3
	v_cvt_pk_f16_f32 v13, v4, v5
	v_lshl_add_u64 v[2:3], v[30:31], 0, s[14:15]
	s_addc_u32 s29, s21, 0
	v_lshlrev_b32_e32 v92, 2, v1
	global_store_dwordx4 v[74:75], v[78:81], off
	global_store_dwordx4 v[58:59], v[62:65], off
	global_store_dwordx4 v[46:47], v[42:45], off
	global_store_dwordx4 v[14:15], v[18:21], off
	global_store_dwordx4 v[2:3], v[10:13], off
	v_lshl_add_u64 v[2:3], s[28:29], 0, v[92:93]
	s_mov_b64 s[28:29], 0x1000
	v_lshl_add_u64 v[10:11], v[2:3], 0, s[28:29]
	global_load_dwordx4 v[22:25], v[10:11], off
	global_load_dwordx4 v[14:17], v[10:11], off offset:16
	global_load_dwordx4 v[6:9], v[10:11], off offset:512
	global_load_dwordx4 v[2:5], v[10:11], off offset:528
	s_mov_b32 s25, 1
	s_mov_b32 s26, 15
	s_mov_b32 s14, 2
	s_mov_b32 s15, 0x18000
	s_mov_b32 s2, 0xc000
	s_mov_b32 s27, 0
	v_mov_b32_e32 v10, v93
	v_mov_b32_e32 v11, v93
	v_mov_b32_e32 v12, v93
	v_mov_b32_e32 v13, v93
	v_mov_b32_e32 v18, v93
	v_mov_b32_e32 v19, v93
	v_mov_b32_e32 v20, v93
	v_mov_b32_e32 v21, v93
	v_mov_b32_e32 v26, v93
	v_mov_b32_e32 v27, v93
	v_mov_b32_e32 v28, v93
	v_mov_b32_e32 v29, v93
	v_mov_b32_e32 v34, v93
	v_mov_b32_e32 v35, v93
	v_mov_b32_e32 v36, v93
	v_mov_b32_e32 v37, v93
	v_mov_b32_e32 v42, v93
	v_mov_b32_e32 v43, v93
	v_mov_b32_e32 v44, v93
	v_mov_b32_e32 v45, v93
	v_mov_b32_e32 v50, v93
	v_mov_b32_e32 v51, v93
	v_mov_b32_e32 v52, v93
	v_mov_b32_e32 v53, v93
	v_mov_b32_e32 v62, v93
	v_mov_b32_e32 v63, v93
	v_mov_b32_e32 v64, v93
	v_mov_b32_e32 v65, v93
	v_mov_b32_e32 v70, v93
	v_mov_b32_e32 v71, v93
	v_mov_b32_e32 v72, v93
	v_mov_b32_e32 v73, v93
	v_mov_b32_e32 v30, v93
	v_mov_b32_e32 v31, v93
	v_mov_b32_e32 v32, v93
	v_mov_b32_e32 v33, v93
	v_mov_b32_e32 v38, v93
	v_mov_b32_e32 v39, v93
	v_mov_b32_e32 v40, v93
	v_mov_b32_e32 v41, v93
	v_mov_b32_e32 v46, v93
	v_mov_b32_e32 v47, v93
	v_mov_b32_e32 v48, v93
	v_mov_b32_e32 v49, v93
	v_mov_b32_e32 v54, v93
	v_mov_b32_e32 v55, v93
	v_mov_b32_e32 v56, v93
	v_mov_b32_e32 v57, v93
	v_mov_b32_e32 v58, v93
	v_mov_b32_e32 v59, v93
	v_mov_b32_e32 v60, v93
	v_mov_b32_e32 v61, v93
	v_mov_b32_e32 v66, v93
	v_mov_b32_e32 v67, v93
	v_mov_b32_e32 v68, v93
	v_mov_b32_e32 v69, v93
	v_mov_b32_e32 v74, v93
	v_mov_b32_e32 v75, v93
	v_mov_b32_e32 v76, v93
	v_mov_b32_e32 v77, v93
	v_mov_b32_e32 v78, v93
	v_mov_b32_e32 v79, v93
	v_mov_b32_e32 v80, v93
	v_mov_b32_e32 v81, v93
.LBB1_5:
	s_mov_b32 s28, s2
	v_add_u32_e32 v1, s28, v101
	ds_read_b128 v[106:109], v1 offset:16384
	ds_read_b128 v[110:113], v1 offset:17408
	ds_read_b128 v[114:117], v1 offset:18432
	ds_read_b128 v[118:121], v1 offset:19456
	ds_read_b128 v[122:125], v1 offset:32768
	ds_read_b128 v[126:129], v1 offset:33792
	ds_read_b128 v[130:133], v1 offset:34816
	ds_read_b128 v[134:137], v1 offset:35840
	v_add_u32_e32 v1, s28, v91
	ds_read_b128 v[138:141], v1
	ds_read_b128 v[142:145], v1 offset:1024
	ds_read_b128 v[146:149], v1 offset:2048
	ds_read_b128 v[150:153], v1 offset:3072
	ds_read_b128 v[154:157], v1 offset:4096
	ds_read_b128 v[158:161], v1 offset:5120
	ds_read_b128 v[162:165], v1 offset:6144
	ds_read_b128 v[166:169], v1 offset:7168
	s_lshl_b32 s2, s25, 2
	s_or_b32 s2, s2, s23
	s_lshl_b64 s[30:31], s[2:3], 19
	s_add_u32 s2, s6, s30
	s_addc_u32 s29, s7, s31
	s_lshl_b32 s33, s14, 7
	s_ashr_i32 s35, s33, 31
	s_add_u32 s30, s2, s33
	s_addc_u32 s31, s29, s35
	s_add_u32 s34, s4, s33
	s_addc_u32 s35, s5, s35
	s_add_i32 s2, s19, s27
	s_add_i32 m0, s2, 0x4000
	s_nop 0
	global_load_lds_dwordx4 v84, s[30:31]
	s_add_i32 m0, s2, 0x6000
	s_nop 0
	global_load_lds_dwordx4 v88, s[30:31]
	s_mov_b32 m0, s2
	s_nop 0
	global_load_lds_dwordx4 v82, s[34:35]
	s_waitcnt vmcnt(3)
	s_waitcnt lgkmcnt(0)
	s_barrier
	s_setprio 1
	s_waitcnt lgkmcnt(0)
	v_mfma_f32_16x16x32_f16 v[78:81], v[106:109], v[138:141], v[78:81]
	s_add_i32 m0, s2, 0x8000
	v_mfma_f32_16x16x32_f16 v[74:77], v[114:117], v[138:141], v[74:77]
	global_load_lds_dwordx4 v172, s[30:31]
	s_add_i32 m0, s2, 0xa000
	v_mfma_f32_16x16x32_f16 v[66:69], v[106:109], v[146:149], v[66:69]
	global_load_lds_dwordx4 v173, s[30:31]
	s_add_i32 m0, s2, 0x2000
	v_mfma_f32_16x16x32_f16 v[58:61], v[114:117], v[146:149], v[58:61]
	global_load_lds_dwordx4 v86, s[34:35]
	v_mfma_f32_16x16x32_f16 v[78:81], v[110:113], v[142:145], v[78:81]
	v_mfma_f32_16x16x32_f16 v[74:77], v[118:121], v[142:145], v[74:77]
	v_mfma_f32_16x16x32_f16 v[66:69], v[110:113], v[150:153], v[66:69]
	v_mfma_f32_16x16x32_f16 v[58:61], v[118:121], v[150:153], v[58:61]
	v_mfma_f32_16x16x32_f16 v[54:57], v[106:109], v[154:157], v[54:57]
	v_mfma_f32_16x16x32_f16 v[46:49], v[114:117], v[154:157], v[46:49]
	v_mfma_f32_16x16x32_f16 v[38:41], v[106:109], v[162:165], v[38:41]
	v_mfma_f32_16x16x32_f16 v[30:33], v[114:117], v[162:165], v[30:33]
	v_mfma_f32_16x16x32_f16 v[54:57], v[110:113], v[158:161], v[54:57]
	v_mfma_f32_16x16x32_f16 v[46:49], v[118:121], v[158:161], v[46:49]
	v_mfma_f32_16x16x32_f16 v[38:41], v[110:113], v[166:169], v[38:41]
	v_mfma_f32_16x16x32_f16 v[30:33], v[118:121], v[166:169], v[30:33]
	v_mfma_f32_16x16x32_f16 v[70:73], v[122:125], v[138:141], v[70:73]
	v_mfma_f32_16x16x32_f16 v[62:65], v[130:133], v[138:141], v[62:65]
	v_mfma_f32_16x16x32_f16 v[50:53], v[122:125], v[146:149], v[50:53]
	v_mfma_f32_16x16x32_f16 v[42:45], v[130:133], v[146:149], v[42:45]
	v_mfma_f32_16x16x32_f16 v[70:73], v[126:129], v[142:145], v[70:73]
	v_mfma_f32_16x16x32_f16 v[62:65], v[134:137], v[142:145], v[62:65]
	v_mfma_f32_16x16x32_f16 v[50:53], v[126:129], v[150:153], v[50:53]
	v_mfma_f32_16x16x32_f16 v[42:45], v[134:137], v[150:153], v[42:45]
	v_mfma_f32_16x16x32_f16 v[34:37], v[122:125], v[154:157], v[34:37]
	v_mfma_f32_16x16x32_f16 v[26:29], v[130:133], v[154:157], v[26:29]
	s_add_i32 s14, s14, 1
	s_bitcmp1_b32 s14, 4
	s_addc_u32 s25, s25, 0
	v_mfma_f32_16x16x32_f16 v[18:21], v[122:125], v[162:165], v[18:21]
	s_and_b32 s14, s14, 15
	v_mfma_f32_16x16x32_f16 v[10:13], v[130:133], v[162:165], v[10:13]
	v_mfma_f32_16x16x32_f16 v[34:37], v[126:129], v[158:161], v[34:37]
	v_mfma_f32_16x16x32_f16 v[26:29], v[134:137], v[158:161], v[26:29]
	v_mfma_f32_16x16x32_f16 v[18:21], v[126:129], v[166:169], v[18:21]
	s_mov_b32 s2, s15
	s_mov_b32 s15, s27
	v_mfma_f32_16x16x32_f16 v[10:13], v[134:137], v[166:169], v[10:13]
	s_mov_b32 s27, s28
	s_add_u32 s26, s26, -1
	s_setprio 0
	s_barrier
	s_cbranch_scc1 .LBB1_5
	s_ashr_i32 s2, s17, 7
	s_and_b32 s3, s2, -16
	s_or_b32 s2, s3, 2
	s_sub_u32 s14, s10, s8
	s_subb_u32 s11, s11, s9
	s_bfe_u32 s6, s17, 0x50006
	s_add_u32 s14, s8, s14
	s_addc_u32 s15, s9, s11
	s_lshr_b32 s11, s24, 6
	s_or_b32 s17, s11, s3
	s_lshl_b32 s17, s17, 8
	s_lshl_b32 s23, s6, 3
	v_bfe_u32 v93, v105, 3, 3
	v_pk_add_f32 v[80:81], v[24:25], v[80:81]
	v_pk_add_f32 v[78:79], v[22:23], v[78:79]
	v_pk_add_f32 v[74:75], v[14:15], v[74:75]
	s_or_b32 s17, s17, s23
	s_or_b32 s11, s2, s11
	v_cvt_pk_f16_f32 v78, v78, v79
	v_cvt_pk_f16_f32 v79, v80, v81
	v_cvt_pk_f16_f32 v80, v74, v75
	v_or_b32_e32 v74, s17, v93
	s_lshl_b32 s11, s11, 8
	v_ashrrev_i32_e32 v75, 31, v74
	v_pk_add_f32 v[72:73], v[8:9], v[72:73]
	v_pk_add_f32 v[70:71], v[6:7], v[70:71]
	v_pk_add_f32 v[62:63], v[2:3], v[62:63]
	s_or_b32 s11, s11, s23
	v_lshlrev_b64 v[74:75], 10, v[74:75]
	v_cvt_pk_f16_f32 v70, v70, v71
	v_cvt_pk_f16_f32 v71, v72, v73
	v_cvt_pk_f16_f32 v72, v62, v63
	v_or_b32_e32 v62, s11, v93
	v_pk_add_f32 v[76:77], v[16:17], v[76:77]
	v_lshl_add_u64 v[74:75], s[14:15], 0, v[74:75]
	v_ashrrev_i32_e32 v63, 31, v62
	v_cvt_pk_f16_f32 v81, v76, v77
	v_lshl_add_u64 v[76:77], v[74:75], 0, v[98:99]
	v_lshlrev_b64 v[62:63], 10, v[62:63]
	global_store_dwordx4 v[76:77], v[78:81], off
	v_pk_add_f32 v[64:65], v[4:5], v[64:65]
	v_lshl_add_u64 v[76:77], s[14:15], 0, v[62:63]
	v_cvt_pk_f16_f32 v73, v64, v65
	v_lshl_add_u64 v[62:63], v[76:77], 0, v[98:99]
	global_store_dwordx4 v[62:63], v[70:73], off
	v_pk_add_f32 v[64:65], v[24:25], v[68:69]
	v_pk_add_f32 v[62:63], v[22:23], v[66:67]
	v_pk_add_f32 v[60:61], v[16:17], v[60:61]
	v_pk_add_f32 v[58:59], v[14:15], v[58:59]
	v_pk_add_f32 v[52:53], v[8:9], v[52:53]
	v_pk_add_f32 v[50:51], v[6:7], v[50:51]
	v_pk_add_f32 v[44:45], v[4:5], v[44:45]
	v_pk_add_f32 v[42:43], v[2:3], v[42:43]
	v_cvt_pk_f16_f32 v62, v62, v63
	v_cvt_pk_f16_f32 v63, v64, v65
	v_cvt_pk_f16_f32 v64, v58, v59
	v_cvt_pk_f16_f32 v65, v60, v61
	v_lshl_add_u64 v[58:59], v[74:75], 0, v[96:97]
	v_cvt_pk_f16_f32 v50, v50, v51
	v_cvt_pk_f16_f32 v51, v52, v53
	v_cvt_pk_f16_f32 v52, v42, v43
	v_cvt_pk_f16_f32 v53, v44, v45
	v_lshl_add_u64 v[42:43], v[76:77], 0, v[96:97]
	v_mov_b32_e32 v1, 0
	global_store_dwordx4 v[58:59], v[62:65], off
	global_store_dwordx4 v[42:43], v[50:53], off
	v_pk_add_f32 v[44:45], v[24:25], v[56:57]
	v_pk_add_f32 v[42:43], v[22:23], v[54:55]
	v_mov_b32_e32 v95, v1
	v_cvt_pk_f16_f32 v42, v42, v43
	v_cvt_pk_f16_f32 v43, v44, v45
	v_pk_add_f32 v[48:49], v[16:17], v[48:49]
	v_pk_add_f32 v[44:45], v[14:15], v[46:47]
	v_pk_add_f32 v[36:37], v[8:9], v[36:37]
	v_pk_add_f32 v[34:35], v[6:7], v[34:35]
	v_pk_add_f32 v[28:29], v[4:5], v[28:29]
	v_pk_add_f32 v[26:27], v[2:3], v[26:27]
	v_pk_add_f32 v[24:25], v[24:25], v[40:41]
	v_pk_add_f32 v[22:23], v[22:23], v[38:39]
	v_pk_add_f32 v[16:17], v[16:17], v[32:33]
	v_pk_add_f32 v[14:15], v[14:15], v[30:31]
	v_pk_add_f32 v[8:9], v[8:9], v[20:21]
	v_pk_add_f32 v[6:7], v[6:7], v[18:19]
	v_pk_add_f32 v[4:5], v[4:5], v[12:13]
	v_pk_add_f32 v[2:3], v[2:3], v[10:11]
	s_add_u32 s14, s20, s22
	v_cvt_pk_f16_f32 v44, v44, v45
	v_cvt_pk_f16_f32 v45, v48, v49
	v_lshl_add_u64 v[46:47], v[74:75], 0, v[0:1]
	v_cvt_pk_f16_f32 v34, v34, v35
	v_cvt_pk_f16_f32 v35, v36, v37
	v_cvt_pk_f16_f32 v36, v26, v27
	v_cvt_pk_f16_f32 v37, v28, v29
	v_lshl_add_u64 v[26:27], v[76:77], 0, v[0:1]
	v_cvt_pk_f16_f32 v22, v22, v23
	v_cvt_pk_f16_f32 v23, v24, v25
	v_cvt_pk_f16_f32 v24, v14, v15
	v_cvt_pk_f16_f32 v25, v16, v17
	v_lshl_add_u64 v[14:15], v[74:75], 0, v[94:95]
	v_cvt_pk_f16_f32 v6, v6, v7
	v_cvt_pk_f16_f32 v7, v8, v9
	v_cvt_pk_f16_f32 v8, v2, v3
	v_cvt_pk_f16_f32 v9, v4, v5
	v_lshl_add_u64 v[2:3], v[76:77], 0, v[94:95]
	s_addc_u32 s15, s21, 0
	v_mov_b32_e32 v93, v1
	global_store_dwordx4 v[46:47], v[42:45], off
	global_store_dwordx4 v[26:27], v[34:37], off
	global_store_dwordx4 v[14:15], v[22:25], off
	global_store_dwordx4 v[2:3], v[6:9], off
	v_lshl_add_u64 v[2:3], s[14:15], 0, v[92:93]
	s_mov_b64 s[14:15], 0x2000
	v_lshl_add_u64 v[2:3], v[2:3], 0, s[14:15]
	global_load_dwordx4 v[20:23], v[2:3], off
	global_load_dwordx4 v[12:15], v[2:3], off offset:16
	global_load_dwordx4 v[8:11], v[2:3], off offset:512
	global_load_dwordx4 v[4:7], v[2:3], off offset:528
	s_add_u32 s11, s12, 0x400000
	s_mov_b32 s7, 2
	v_and_b32_e32 v106, 56, v105
	s_mov_b32 s10, 0
	s_addc_u32 s12, s13, 0
	s_mov_b32 s14, 0xc000
	s_mov_b32 s17, 0x18000
	s_mov_b32 s13, 15
	v_mov_b32_e32 v0, v1
	v_mov_b32_e32 v2, v1
	v_mov_b32_e32 v3, v1
	v_mov_b32_e32 v16, v1
	v_mov_b32_e32 v17, v1
	v_mov_b32_e32 v18, v1
	v_mov_b32_e32 v19, v1
	v_mov_b32_e32 v24, v1
	v_mov_b32_e32 v25, v1
	v_mov_b32_e32 v26, v1
	v_mov_b32_e32 v27, v1
	v_mov_b32_e32 v32, v1
	v_mov_b32_e32 v33, v1
	v_mov_b32_e32 v34, v1
	v_mov_b32_e32 v35, v1
	v_mov_b32_e32 v40, v1
	v_mov_b32_e32 v41, v1
	v_mov_b32_e32 v42, v1
	v_mov_b32_e32 v43, v1
	v_mov_b32_e32 v48, v1
	v_mov_b32_e32 v49, v1
	v_mov_b32_e32 v50, v1
	v_mov_b32_e32 v51, v1
	v_mov_b32_e32 v60, v1
	v_mov_b32_e32 v61, v1
	v_mov_b32_e32 v62, v1
	v_mov_b32_e32 v63, v1
	v_mov_b32_e32 v68, v1
	v_mov_b32_e32 v69, v1
	v_mov_b32_e32 v70, v1
	v_mov_b32_e32 v71, v1
	v_mov_b32_e32 v28, v1
	v_mov_b32_e32 v29, v1
	v_mov_b32_e32 v30, v1
	v_mov_b32_e32 v31, v1
	v_mov_b32_e32 v36, v1
	v_mov_b32_e32 v37, v1
	v_mov_b32_e32 v38, v1
	v_mov_b32_e32 v39, v1
	v_mov_b32_e32 v44, v1
	v_mov_b32_e32 v45, v1
	v_mov_b32_e32 v46, v1
	v_mov_b32_e32 v47, v1
	v_mov_b32_e32 v52, v1
	v_mov_b32_e32 v53, v1
	v_mov_b32_e32 v54, v1
	v_mov_b32_e32 v55, v1
	v_mov_b32_e32 v56, v1
	v_mov_b32_e32 v57, v1
	v_mov_b32_e32 v58, v1
	v_mov_b32_e32 v59, v1
	v_mov_b32_e32 v64, v1
	v_mov_b32_e32 v65, v1
	v_mov_b32_e32 v66, v1
	v_mov_b32_e32 v67, v1
	v_mov_b32_e32 v72, v1
	v_mov_b32_e32 v73, v1
	v_mov_b32_e32 v74, v1
	v_mov_b32_e32 v75, v1
	v_mov_b32_e32 v76, v1
	v_mov_b32_e32 v77, v1
	v_mov_b32_e32 v78, v1
	v_mov_b32_e32 v79, v1
.LBB1_7:
	s_mov_b32 s15, s17
	v_add_u32_e32 v80, s15, v101
	ds_read_b128 v[92:95], v80 offset:16384
	ds_read_b128 v[96:99], v80 offset:17408
	ds_read_b128 v[108:111], v80 offset:18432
	ds_read_b128 v[112:115], v80 offset:19456
	ds_read_b128 v[116:119], v80 offset:32768
	ds_read_b128 v[120:123], v80 offset:33792
	ds_read_b128 v[124:127], v80 offset:34816
	ds_read_b128 v[128:131], v80 offset:35840
	v_add_u32_e32 v80, s15, v91
	ds_read_b128 v[132:135], v80
	ds_read_b128 v[136:139], v80 offset:1024
	ds_read_b128 v[140:143], v80 offset:2048
	ds_read_b128 v[144:147], v80 offset:3072
	ds_read_b128 v[148:151], v80 offset:4096
	ds_read_b128 v[152:155], v80 offset:5120
	ds_read_b128 v[156:159], v80 offset:6144
	ds_read_b128 v[160:163], v80 offset:7168
	s_lshl_b32 s17, s7, 7
	s_ashr_i32 s23, s17, 31
	s_add_u32 s20, s11, s17
	s_addc_u32 s21, s12, s23
	s_add_u32 s22, s4, s17
	s_addc_u32 s23, s5, s23
	s_add_i32 s17, s19, s14
	s_add_i32 m0, s17, 0x4000
	s_nop 0
	global_load_lds_dwordx4 v84, s[20:21]
	s_add_i32 m0, s17, 0x6000
	s_nop 0
	global_load_lds_dwordx4 v88, s[20:21]
	s_mov_b32 m0, s17
	s_nop 0
	global_load_lds_dwordx4 v82, s[22:23]
	s_waitcnt vmcnt(3)
	s_waitcnt lgkmcnt(0)
	s_barrier
	s_setprio 1
	s_waitcnt lgkmcnt(0)
	v_mfma_f32_16x16x32_f16 v[76:79], v[92:95], v[132:135], v[76:79]
	s_add_i32 m0, s17, 0x8000
	v_mfma_f32_16x16x32_f16 v[72:75], v[108:111], v[132:135], v[72:75]
	global_load_lds_dwordx4 v172, s[20:21]
	s_add_i32 m0, s17, 0xa000
	v_mfma_f32_16x16x32_f16 v[64:67], v[92:95], v[140:143], v[64:67]
	global_load_lds_dwordx4 v173, s[20:21]
	s_add_i32 m0, s17, 0x2000
	v_mfma_f32_16x16x32_f16 v[56:59], v[108:111], v[140:143], v[56:59]
	global_load_lds_dwordx4 v86, s[22:23]
	v_mfma_f32_16x16x32_f16 v[76:79], v[96:99], v[136:139], v[76:79]
	v_mfma_f32_16x16x32_f16 v[72:75], v[112:115], v[136:139], v[72:75]
	v_mfma_f32_16x16x32_f16 v[64:67], v[96:99], v[144:147], v[64:67]
	v_mfma_f32_16x16x32_f16 v[56:59], v[112:115], v[144:147], v[56:59]
	v_mfma_f32_16x16x32_f16 v[52:55], v[92:95], v[148:151], v[52:55]
	v_mfma_f32_16x16x32_f16 v[44:47], v[108:111], v[148:151], v[44:47]
	v_mfma_f32_16x16x32_f16 v[36:39], v[92:95], v[156:159], v[36:39]
	v_mfma_f32_16x16x32_f16 v[28:31], v[108:111], v[156:159], v[28:31]
	v_mfma_f32_16x16x32_f16 v[52:55], v[96:99], v[152:155], v[52:55]
	v_mfma_f32_16x16x32_f16 v[44:47], v[112:115], v[152:155], v[44:47]
	v_mfma_f32_16x16x32_f16 v[36:39], v[96:99], v[160:163], v[36:39]
	v_mfma_f32_16x16x32_f16 v[28:31], v[112:115], v[160:163], v[28:31]
	v_mfma_f32_16x16x32_f16 v[68:71], v[116:119], v[132:135], v[68:71]
	v_mfma_f32_16x16x32_f16 v[60:63], v[124:127], v[132:135], v[60:63]
	v_mfma_f32_16x16x32_f16 v[48:51], v[116:119], v[140:143], v[48:51]
	v_mfma_f32_16x16x32_f16 v[40:43], v[124:127], v[140:143], v[40:43]
	v_mfma_f32_16x16x32_f16 v[68:71], v[120:123], v[136:139], v[68:71]
	v_mfma_f32_16x16x32_f16 v[60:63], v[128:131], v[136:139], v[60:63]
	v_mfma_f32_16x16x32_f16 v[48:51], v[120:123], v[144:147], v[48:51]
	v_mfma_f32_16x16x32_f16 v[40:43], v[128:131], v[144:147], v[40:43]
	v_mfma_f32_16x16x32_f16 v[32:35], v[116:119], v[148:151], v[32:35]
	v_mfma_f32_16x16x32_f16 v[24:27], v[124:127], v[148:151], v[24:27]
	s_add_i32 s7, s7, 1
	s_and_b32 s7, s7, 15
	v_mfma_f32_16x16x32_f16 v[16:19], v[116:119], v[156:159], v[16:19]
	v_mfma_f32_16x16x32_f16 v[0:3], v[124:127], v[156:159], v[0:3]
	v_mfma_f32_16x16x32_f16 v[32:35], v[120:123], v[152:155], v[32:35]
	s_mov_b32 s17, s10
	v_mfma_f32_16x16x32_f16 v[24:27], v[128:131], v[152:155], v[24:27]
	s_mov_b32 s10, s14
	v_mfma_f32_16x16x32_f16 v[16:19], v[120:123], v[160:163], v[16:19]
	s_mov_b32 s14, s15
	v_mfma_f32_16x16x32_f16 v[0:3], v[128:131], v[160:163], v[0:3]
	s_add_u32 s13, s13, -1
	s_setprio 0
	s_barrier
	s_cbranch_scc1 .LBB1_7
	s_sub_u32 s0, s0, s8
	s_subb_u32 s1, s1, s9
	s_add_u32 s0, s8, s0
	s_addc_u32 s1, s9, s1
	s_lshl_b32 s3, s3, 6
	s_or_b32 s3, s3, s16
	s_lshl_b32 s4, s6, 1
	v_lshrrev_b32_e32 v86, 5, v106
	v_pk_add_f32 v[78:79], v[22:23], v[78:79]
	v_pk_add_f32 v[76:77], v[20:21], v[76:77]
	v_pk_add_f32 v[72:73], v[12:13], v[72:73]
	s_or_b32 s3, s3, s4
	s_lshl_b32 s2, s2, 6
	v_cvt_pk_f16_f32 v76, v76, v77
	v_cvt_pk_f16_f32 v77, v78, v79
	v_cvt_pk_f16_f32 v78, v72, v73
	v_or_b32_e32 v72, s3, v86
	s_or_b32 s2, s2, s16
	v_ashrrev_i32_e32 v73, 31, v72
	v_pk_add_f32 v[70:71], v[10:11], v[70:71]
	v_pk_add_f32 v[68:69], v[8:9], v[68:69]
	v_pk_add_f32 v[60:61], v[4:5], v[60:61]
	s_or_b32 s2, s2, s4
	v_lshlrev_b64 v[72:73], 12, v[72:73]
	v_cvt_pk_f16_f32 v68, v68, v69
	v_cvt_pk_f16_f32 v69, v70, v71
	v_cvt_pk_f16_f32 v70, v60, v61
	v_or_b32_e32 v60, s2, v86
	v_mov_b32_e32 v91, 0
	v_pk_add_f32 v[74:75], v[14:15], v[74:75]
	v_lshl_add_u64 v[72:73], s[0:1], 0, v[72:73]
	v_ashrrev_i32_e32 v61, 31, v60
	v_cvt_pk_f16_f32 v79, v74, v75
	v_lshl_add_u64 v[74:75], v[72:73], 0, v[90:91]
	v_lshlrev_b64 v[60:61], 12, v[60:61]
	v_lshl_or_b32 v84, v102, 6, v100
	v_mov_b32_e32 v85, v91
	global_store_dwordx4 v[74:75], v[76:79], off sc1
	v_lshl_add_u64 v[74:75], s[0:1], 0, v[60:61]
	v_pk_add_f32 v[50:51], v[10:11], v[50:51]
	v_pk_add_f32 v[48:49], v[8:9], v[48:49]
	v_pk_add_f32 v[42:43], v[6:7], v[42:43]
	v_pk_add_f32 v[40:41], v[4:5], v[40:41]
	v_pk_add_f32 v[62:63], v[6:7], v[62:63]
	v_cvt_pk_f16_f32 v48, v48, v49
	v_cvt_pk_f16_f32 v49, v50, v51
	v_cvt_pk_f16_f32 v50, v40, v41
	v_cvt_pk_f16_f32 v51, v42, v43
	v_lshl_add_u64 v[40:41], v[74:75], 0, v[84:85]
	v_cvt_pk_f16_f32 v71, v62, v63
	v_lshl_add_u64 v[60:61], v[74:75], 0, v[90:91]
	global_store_dwordx4 v[40:41], v[48:51], off sc1
	v_pk_add_f32 v[42:43], v[22:23], v[54:55]
	v_pk_add_f32 v[40:41], v[20:21], v[52:53]
	v_lshl_or_b32 v80, v103, 6, v100
	v_lshl_or_b32 v82, v104, 6, v100
	v_mov_b32_e32 v81, v91
	v_mov_b32_e32 v83, v91
	global_store_dwordx4 v[60:61], v[68:71], off sc1
	v_pk_add_f32 v[62:63], v[22:23], v[66:67]
	v_pk_add_f32 v[60:61], v[20:21], v[64:65]
	v_pk_add_f32 v[58:59], v[14:15], v[58:59]
	v_pk_add_f32 v[56:57], v[12:13], v[56:57]
	v_cvt_pk_f16_f32 v40, v40, v41
	v_cvt_pk_f16_f32 v41, v42, v43
	v_pk_add_f32 v[46:47], v[14:15], v[46:47]
	v_pk_add_f32 v[42:43], v[12:13], v[44:45]
	v_pk_add_f32 v[34:35], v[10:11], v[34:35]
	v_pk_add_f32 v[32:33], v[8:9], v[32:33]
	v_pk_add_f32 v[26:27], v[6:7], v[26:27]
	v_pk_add_f32 v[24:25], v[4:5], v[24:25]
	v_pk_add_f32 v[22:23], v[22:23], v[38:39]
	v_pk_add_f32 v[20:21], v[20:21], v[36:37]
	v_pk_add_f32 v[14:15], v[14:15], v[30:31]
	v_pk_add_f32 v[12:13], v[12:13], v[28:29]
	v_pk_add_f32 v[10:11], v[10:11], v[18:19]
	v_pk_add_f32 v[8:9], v[8:9], v[16:17]
	v_pk_add_f32 v[2:3], v[6:7], v[2:3]
	v_pk_add_f32 v[0:1], v[4:5], v[0:1]
	v_cvt_pk_f16_f32 v60, v60, v61
	v_cvt_pk_f16_f32 v61, v62, v63
	v_cvt_pk_f16_f32 v62, v56, v57
	v_cvt_pk_f16_f32 v63, v58, v59
	v_lshl_add_u64 v[56:57], v[72:73], 0, v[84:85]
	v_cvt_pk_f16_f32 v42, v42, v43
	v_cvt_pk_f16_f32 v43, v46, v47
	v_lshl_add_u64 v[44:45], v[72:73], 0, v[80:81]
	v_cvt_pk_f16_f32 v32, v32, v33
	v_cvt_pk_f16_f32 v33, v34, v35
	v_cvt_pk_f16_f32 v34, v24, v25
	v_cvt_pk_f16_f32 v35, v26, v27
	v_lshl_add_u64 v[24:25], v[74:75], 0, v[80:81]
	v_cvt_pk_f16_f32 v20, v20, v21
	v_cvt_pk_f16_f32 v21, v22, v23
	v_cvt_pk_f16_f32 v22, v12, v13
	v_cvt_pk_f16_f32 v23, v14, v15
	v_lshl_add_u64 v[12:13], v[72:73], 0, v[82:83]
	v_cvt_pk_f16_f32 v8, v8, v9
	v_cvt_pk_f16_f32 v9, v10, v11
	v_cvt_pk_f16_f32 v10, v0, v1
	v_cvt_pk_f16_f32 v11, v2, v3
	v_lshl_add_u64 v[0:1], v[74:75], 0, v[82:83]
	global_store_dwordx4 v[56:57], v[60:63], off sc1
	global_store_dwordx4 v[44:45], v[40:43], off sc1
	global_store_dwordx4 v[24:25], v[32:35], off sc1
	global_store_dwordx4 v[12:13], v[20:23], off sc1
	global_store_dwordx4 v[0:1], v[8:11], off sc1
	s_waitcnt vmcnt(0)
	s_cmpk_gt_u32 s18, 0xff
	s_cbranch_scc1 .LBB1_10
	s_barrier

	.amdhsa_kernel _Z10kvq_kernelPKtS0_PtS1_S1_PKf
		.amdhsa_group_segment_fixed_size 0
		.amdhsa_private_segment_fixed_size 0
		.amdhsa_kernarg_size 48
		.amdhsa_user_sgpr_count 2
		.amdhsa_user_sgpr_dispatch_ptr 0
		.amdhsa_user_sgpr_queue_ptr 0
		.amdhsa_user_sgpr_kernarg_segment_ptr 1
		.amdhsa_user_sgpr_dispatch_id 0
		.amdhsa_user_sgpr_kernarg_preload_length 0
		.amdhsa_user_sgpr_kernarg_preload_offset 0
		.amdhsa_user_sgpr_private_segment_size 0
		.amdhsa_uses_dynamic_stack 0
		.amdhsa_enable_private_segment 0
		.amdhsa_system_sgpr_workgroup_id_x 1
		.amdhsa_system_sgpr_workgroup_id_y 0
		.amdhsa_system_sgpr_workgroup_id_z 0
		.amdhsa_system_sgpr_workgroup_info 0
		.amdhsa_system_vgpr_workitem_id 0
		.amdhsa_next_free_vgpr 176
		.amdhsa_next_free_sgpr 38
		.amdhsa_accum_offset 176
		.amdhsa_reserve_vcc 0
		.amdhsa_float_round_mode_32 0
		.amdhsa_float_round_mode_16_64 0
		.amdhsa_float_denorm_mode_32 3
		.amdhsa_float_denorm_mode_16_64 3
		.amdhsa_dx10_clamp 1
		.amdhsa_ieee_mode 1
		.amdhsa_fp16_overflow 0
		.amdhsa_tg_split 0
		.amdhsa_exception_fp_ieee_invalid_op 0
		.amdhsa_exception_fp_denorm_src 0
		.amdhsa_exception_fp_ieee_div_zero 0
		.amdhsa_exception_fp_ieee_overflow 0
		.amdhsa_exception_fp_ieee_underflow 0
		.amdhsa_exception_fp_ieee_inexact 0
		.amdhsa_exception_int_div_zero 0
	.end_amdhsa_kernel

_Z11out2_kernelPKtS0_PfPKf:
	s_load_dwordx8 s[4:11], s[0:1], 0x0
	s_ashr_i32 s0, s2, 31
	s_lshr_b32 s0, s0, 29
	s_add_i32 s0, s2, s0
	s_ashr_i32 s1, s0, 3
	s_lshl_b32 s0, s2, 5
	s_mul_i32 s2, s1, 0xffffff01
	s_add_i32 s2, s2, s0
	s_ashr_i32 s0, s2, 2
	v_lshlrev_b32_e32 v1, 4, v0
	v_and_b32_e32 v2, 32, v0
	s_and_b32 s0, s0, -8
	s_and_b32 s2, s1, 7
	v_bfe_u32 v3, v0, 2, 4
	v_bitop3_b32 v1, v1, v2, 48 bitop3:0x6c
	v_lshrrev_b32_e32 v2, 3, v0
	s_or_b32 s0, s0, s2
	s_bfe_u32 s16, s1, 0x20003
	v_and_or_b32 v4, v2, 48, v3
	v_or_b32_e32 v2, 64, v2
	s_movk_i32 s1, 0x70
	v_readfirstlane_b32 s12, v0
	v_and_or_b32 v2, v2, s1, v3
	s_ashr_i32 s1, s0, 31
	s_lshr_b32 s14, s12, 8
	s_lshl_b64 s[2:3], s[0:1], 18
	s_waitcnt lgkmcnt(0)
	s_add_u32 s2, s4, s2
	s_addc_u32 s3, s5, s3
	s_lshr_b32 s1, s12, 1
	s_lshl_b32 s4, s12, 4
	s_and_b32 s13, s4, 0xfffffc00
	s_and_b32 s1, s1, 0x60
	s_lshl_b32 s4, s16, 19
	s_add_u32 s4, s6, s4
	v_and_or_b32 v1, v0, 64, v1
	s_addc_u32 s5, s7, 0
	s_add_i32 s6, s13, 0
	v_lshl_or_b32 v82, v4, 11, v1
	s_add_i32 m0, s6, 0x4000
	v_lshl_or_b32 v84, v2, 11, v1
	v_add_u32_e32 v156, 0x40000, v82
	v_add_u32_e32 v157, 0x40000, v84
	global_load_lds_dwordx4 v82, s[4:5]
	s_add_i32 m0, s6, 0x6000
	s_add_u32 s18, s4, 0x40000
	global_load_lds_dwordx4 v84, s[4:5]
	s_mov_b32 m0, s6
	v_mov_b32_e32 v18, 0
	global_load_lds_dwordx4 v82, s[2:3]
	s_addc_u32 s19, s5, 0
	s_add_i32 m0, s6, 0x8000
	v_mov_b32_e32 v83, v18
	global_load_lds_dwordx4 v82, s[18:19]
	s_add_i32 m0, s6, 0xa000
	v_lshl_add_u64 v[2:3], s[4:5], 0, v[82:83]
	v_mov_b32_e32 v85, v18
	global_load_lds_dwordx4 v84, s[18:19]
	s_add_i32 m0, s6, 0x2000
	s_mov_b64 s[18:19], 0x80
	v_lshl_add_u64 v[4:5], s[4:5], 0, v[84:85]
	global_load_lds_dwordx4 v84, s[2:3]
	v_lshl_add_u64 v[2:3], v[2:3], 0, s[18:19]
	s_add_i32 m0, s6, 0x10000
	v_lshl_add_u64 v[6:7], s[2:3], 0, v[82:83]
	global_load_lds_dwordx4 v[2:3], off
	v_lshl_add_u64 v[2:3], v[4:5], 0, s[18:19]
	s_add_i32 m0, s6, 0x12000
	v_lshl_add_u64 v[8:9], s[2:3], 0, v[84:85]
	global_load_lds_dwordx4 v[2:3], off
	s_add_i32 m0, s6, 0xc000
	v_lshl_add_u64 v[2:3], v[6:7], 0, s[18:19]
	s_add_u32 s20, s4, 0x40080
	global_load_lds_dwordx4 v[2:3], off
	s_addc_u32 s21, s5, 0
	s_add_i32 m0, s6, 0x14000
	v_lshl_add_u64 v[2:3], v[8:9], 0, s[18:19]
	global_load_lds_dwordx4 v82, s[20:21]
	s_add_i32 m0, s6, 0x16000
	s_lshl_b32 s17, s16, 10
	global_load_lds_dwordx4 v84, s[20:21]
	s_add_i32 m0, s6, 0xe000
	s_add_u32 s10, s10, s17
	global_load_lds_dwordx4 v[2:3], off
	s_addc_u32 s11, s11, 0
	s_lshl_b32 s17, s1, 2
	v_bfe_u32 v1, v0, 4, 2
	s_add_u32 s10, s10, s17
	s_addc_u32 s11, s11, 0
	v_lshlrev_b32_e32 v20, 4, v1
	v_mov_b32_e32 v21, v18
	v_lshl_add_u64 v[22:23], s[10:11], 0, v[20:21]
	global_load_dwordx4 v[14:17], v[22:23], off
	global_load_dwordx4 v[10:13], v[22:23], off offset:64
	global_load_dwordx4 v[6:9], v[22:23], off offset:512
	global_load_dwordx4 v[2:5], v[22:23], off offset:576
	s_waitcnt vmcnt(6)
	s_mov_b32 s7, 2
	s_mov_b32 s15, 0
	s_mov_b32 s13, 0xc000
	s_cmp_lg_u32 s14, 1
	s_cbranch_scc1 .LBB2_2
	s_barrier
.LBB2_2:
	v_and_b32_e32 v19, 15, v0
	v_lshlrev_b32_e32 v21, 6, v0
	s_movk_i32 s11, 0x3c0
	v_lshlrev_b32_e32 v0, 2, v0
	s_lshl_b32 s10, s16, 8
	v_lshlrev_b32_e32 v1, 2, v1
	v_lshl_or_b32 v86, s14, 6, v19
	v_lshl_or_b32 v19, v19, 6, v20
	v_and_or_b32 v20, v21, s11, v20
	v_and_b32_e32 v21, 32, v0
	s_lshl_b32 s11, s14, 13
	s_lshl_b32 s14, s1, 7
	s_barrier
	s_add_i32 s11, s11, 0
	s_add_i32 s14, s14, 0
	v_xad_u32 v0, v19, v21, s11
	v_xad_u32 v87, v20, v21, s14
	s_mov_b32 s14, 0x18000
	s_mov_b32 s11, 15
	v_mov_b32_e32 v19, v18
	v_mov_b32_e32 v20, v18
	v_mov_b32_e32 v21, v18
	v_mov_b32_e32 v70, v18
	v_mov_b32_e32 v71, v18
	v_mov_b32_e32 v72, v18
	v_mov_b32_e32 v73, v18
	v_mov_b32_e32 v58, v18
	v_mov_b32_e32 v59, v18
	v_mov_b32_e32 v60, v18
	v_mov_b32_e32 v61, v18
	v_mov_b32_e32 v54, v18
	v_mov_b32_e32 v55, v18
	v_mov_b32_e32 v56, v18
	v_mov_b32_e32 v57, v18
	v_mov_b32_e32 v42, v18
	v_mov_b32_e32 v43, v18
	v_mov_b32_e32 v44, v18
	v_mov_b32_e32 v45, v18
	v_mov_b32_e32 v38, v18
	v_mov_b32_e32 v39, v18
	v_mov_b32_e32 v40, v18
	v_mov_b32_e32 v41, v18
	v_mov_b32_e32 v26, v18
	v_mov_b32_e32 v27, v18
	v_mov_b32_e32 v28, v18
	v_mov_b32_e32 v29, v18
	v_mov_b32_e32 v22, v18
	v_mov_b32_e32 v23, v18
	v_mov_b32_e32 v24, v18
	v_mov_b32_e32 v25, v18
	v_mov_b32_e32 v78, v18
	v_mov_b32_e32 v79, v18
	v_mov_b32_e32 v80, v18
	v_mov_b32_e32 v81, v18
	v_mov_b32_e32 v74, v18
	v_mov_b32_e32 v75, v18
	v_mov_b32_e32 v76, v18
	v_mov_b32_e32 v77, v18
	v_mov_b32_e32 v66, v18
	v_mov_b32_e32 v67, v18
	v_mov_b32_e32 v68, v18
	v_mov_b32_e32 v69, v18
	v_mov_b32_e32 v62, v18
	v_mov_b32_e32 v63, v18
	v_mov_b32_e32 v64, v18
	v_mov_b32_e32 v65, v18
	v_mov_b32_e32 v50, v18
	v_mov_b32_e32 v51, v18
	v_mov_b32_e32 v52, v18
	v_mov_b32_e32 v53, v18
	v_mov_b32_e32 v46, v18
	v_mov_b32_e32 v47, v18
	v_mov_b32_e32 v48, v18
	v_mov_b32_e32 v49, v18
	v_mov_b32_e32 v34, v18
	v_mov_b32_e32 v35, v18
	v_mov_b32_e32 v36, v18
	v_mov_b32_e32 v37, v18
	v_mov_b32_e32 v30, v18
	v_mov_b32_e32 v31, v18
	v_mov_b32_e32 v32, v18
	v_mov_b32_e32 v33, v18
.LBB2_3:
	s_mov_b32 s16, s15
	v_add_u32_e32 v116, s16, v87
	v_add_u32_e32 v148, s16, v0
	ds_read_b128 v[88:91], v116 offset:16384
	ds_read_b128 v[92:95], v116 offset:17408
	ds_read_b128 v[96:99], v116 offset:18432
	ds_read_b128 v[100:103], v116 offset:19456
	ds_read_b128 v[104:107], v116 offset:32768
	ds_read_b128 v[108:111], v116 offset:33792
	ds_read_b128 v[112:115], v116 offset:34816
	ds_read_b128 v[116:119], v116 offset:35840
	ds_read_b128 v[120:123], v148
	ds_read_b128 v[124:127], v148 offset:1024
	ds_read_b128 v[128:131], v148 offset:2048
	ds_read_b128 v[132:135], v148 offset:3072
	ds_read_b128 v[136:139], v148 offset:4096
	ds_read_b128 v[140:143], v148 offset:5120
	ds_read_b128 v[144:147], v148 offset:6144
	ds_read_b128 v[148:151], v148 offset:7168
	s_lshl_b32 s15, s7, 7
	s_ashr_i32 s17, s15, 31
	s_add_u32 s18, s4, s15
	s_addc_u32 s19, s5, s17
	s_add_u32 s20, s2, s15
	s_addc_u32 s21, s3, s17
	s_add_i32 s15, s6, s14
	s_add_i32 m0, s15, 0x4000
	s_nop 0
	global_load_lds_dwordx4 v82, s[18:19]
	s_add_i32 m0, s15, 0x6000
	s_nop 0
	global_load_lds_dwordx4 v84, s[18:19]
	s_mov_b32 m0, s15
	s_nop 0
	global_load_lds_dwordx4 v82, s[20:21]
	s_waitcnt vmcnt(3)
	s_waitcnt lgkmcnt(0)
	s_barrier
	s_setprio 1
	s_waitcnt lgkmcnt(0)
	v_mfma_f32_16x16x32_f16 v[18:21], v[88:91], v[120:123], v[18:21]
	s_add_i32 m0, s15, 0x8000
	v_mfma_f32_16x16x32_f16 v[70:73], v[96:99], v[120:123], v[70:73]
	global_load_lds_dwordx4 v156, s[18:19]
	s_add_i32 m0, s15, 0xa000
	v_mfma_f32_16x16x32_f16 v[58:61], v[88:91], v[128:131], v[58:61]
	global_load_lds_dwordx4 v157, s[18:19]
	s_add_i32 m0, s15, 0x2000
	v_mfma_f32_16x16x32_f16 v[54:57], v[96:99], v[128:131], v[54:57]
	global_load_lds_dwordx4 v84, s[20:21]
	v_mfma_f32_16x16x32_f16 v[18:21], v[92:95], v[124:127], v[18:21]
	v_mfma_f32_16x16x32_f16 v[70:73], v[100:103], v[124:127], v[70:73]
	v_mfma_f32_16x16x32_f16 v[58:61], v[92:95], v[132:135], v[58:61]
	v_mfma_f32_16x16x32_f16 v[54:57], v[100:103], v[132:135], v[54:57]
	v_mfma_f32_16x16x32_f16 v[42:45], v[88:91], v[136:139], v[42:45]
	v_mfma_f32_16x16x32_f16 v[38:41], v[96:99], v[136:139], v[38:41]
	v_mfma_f32_16x16x32_f16 v[26:29], v[88:91], v[144:147], v[26:29]
	v_mfma_f32_16x16x32_f16 v[22:25], v[96:99], v[144:147], v[22:25]
	v_mfma_f32_16x16x32_f16 v[42:45], v[92:95], v[140:143], v[42:45]
	v_mfma_f32_16x16x32_f16 v[38:41], v[100:103], v[140:143], v[38:41]
	v_mfma_f32_16x16x32_f16 v[26:29], v[92:95], v[148:151], v[26:29]
	v_mfma_f32_16x16x32_f16 v[22:25], v[100:103], v[148:151], v[22:25]
	v_mfma_f32_16x16x32_f16 v[78:81], v[104:107], v[120:123], v[78:81]
	v_mfma_f32_16x16x32_f16 v[74:77], v[112:115], v[120:123], v[74:77]
	v_mfma_f32_16x16x32_f16 v[66:69], v[104:107], v[128:131], v[66:69]
	v_mfma_f32_16x16x32_f16 v[62:65], v[112:115], v[128:131], v[62:65]
	v_mfma_f32_16x16x32_f16 v[78:81], v[108:111], v[124:127], v[78:81]
	v_mfma_f32_16x16x32_f16 v[74:77], v[116:119], v[124:127], v[74:77]
	v_mfma_f32_16x16x32_f16 v[66:69], v[108:111], v[132:135], v[66:69]
	v_mfma_f32_16x16x32_f16 v[62:65], v[116:119], v[132:135], v[62:65]
	v_mfma_f32_16x16x32_f16 v[50:53], v[104:107], v[136:139], v[50:53]
	v_mfma_f32_16x16x32_f16 v[46:49], v[112:115], v[136:139], v[46:49]
	s_add_i32 s7, s7, 1
	s_and_b32 s7, s7, 15
	v_mfma_f32_16x16x32_f16 v[34:37], v[104:107], v[144:147], v[34:37]
	v_mfma_f32_16x16x32_f16 v[30:33], v[112:115], v[144:147], v[30:33]
	v_mfma_f32_16x16x32_f16 v[50:53], v[108:111], v[140:143], v[50:53]
	s_mov_b32 s15, s13
	v_mfma_f32_16x16x32_f16 v[46:49], v[116:119], v[140:143], v[46:49]
	s_mov_b32 s13, s14
	v_mfma_f32_16x16x32_f16 v[34:37], v[108:111], v[148:151], v[34:37]
	s_mov_b32 s14, s16
	v_mfma_f32_16x16x32_f16 v[30:33], v[116:119], v[148:151], v[30:33]
	s_add_u32 s11, s11, -1
	s_setprio 0
	s_barrier
	s_cbranch_scc1 .LBB2_3
	v_lshl_add_u32 v0, s0, 7, v86
	v_or_b32_e32 v88, s10, v1
	v_ashrrev_i32_e32 v1, 31, v0
	v_lshlrev_b64 v[82:83], 12, v[0:1]
	v_or_b32_e32 v88, s1, v88
	v_lshl_add_u64 v[82:83], s[8:9], 0, v[82:83]
	v_lshlrev_b32_e32 v88, 2, v88
	v_mov_b32_e32 v89, 0
	v_or_b32_e32 v84, 16, v0
	v_lshl_add_u64 v[82:83], v[82:83], 0, v[88:89]
	v_pk_add_f32 v[20:21], v[16:17], v[20:21]
	v_pk_add_f32 v[18:19], v[14:15], v[18:19]
	v_ashrrev_i32_e32 v85, 31, v84
	global_store_dwordx4 v[82:83], v[18:21], off sc1
	v_lshlrev_b64 v[84:85], 12, v[84:85]
	v_lshl_add_u64 v[84:85], s[8:9], 0, v[84:85]
	v_pk_add_f32 v[20:21], v[12:13], v[72:73]
	v_pk_add_f32 v[18:19], v[10:11], v[70:71]
	global_store_dwordx4 v[82:83], v[18:21], off offset:64 sc1
	v_or_b32_e32 v86, 32, v0
	v_lshl_add_u64 v[84:85], v[84:85], 0, v[88:89]
	v_pk_add_f32 v[20:21], v[8:9], v[80:81]
	v_pk_add_f32 v[18:19], v[6:7], v[78:79]
	global_store_dwordx4 v[82:83], v[18:21], off offset:512 sc1
	v_ashrrev_i32_e32 v87, 31, v86
	v_lshlrev_b64 v[86:87], 12, v[86:87]
	v_pk_add_f32 v[20:21], v[4:5], v[76:77]
	v_pk_add_f32 v[18:19], v[2:3], v[74:75]
	global_store_dwordx4 v[82:83], v[18:21], off offset:576 sc1
	v_lshl_add_u64 v[86:87], s[8:9], 0, v[86:87]
	v_or_b32_e32 v0, 48, v0
	v_pk_add_f32 v[20:21], v[16:17], v[60:61]
	v_pk_add_f32 v[18:19], v[14:15], v[58:59]
	global_store_dwordx4 v[84:85], v[18:21], off sc1
	v_ashrrev_i32_e32 v1, 31, v0
	v_lshl_add_u64 v[86:87], v[86:87], 0, v[88:89]
	v_pk_add_f32 v[20:21], v[12:13], v[56:57]
	v_pk_add_f32 v[18:19], v[10:11], v[54:55]
	global_store_dwordx4 v[84:85], v[18:21], off offset:64 sc1
	v_lshlrev_b64 v[0:1], 12, v[0:1]
	v_lshl_add_u64 v[0:1], s[8:9], 0, v[0:1]
	v_pk_add_f32 v[20:21], v[8:9], v[68:69]
	v_pk_add_f32 v[18:19], v[6:7], v[66:67]
	global_store_dwordx4 v[84:85], v[18:21], off offset:512 sc1
	v_lshl_add_u64 v[0:1], v[0:1], 0, v[88:89]
	s_cmpk_gt_u32 s12, 0xff
	v_pk_add_f32 v[20:21], v[4:5], v[64:65]
	v_pk_add_f32 v[18:19], v[2:3], v[62:63]
	global_store_dwordx4 v[84:85], v[18:21], off offset:576 sc1
	s_nop 1
	v_pk_add_f32 v[20:21], v[16:17], v[44:45]
	v_pk_add_f32 v[18:19], v[14:15], v[42:43]
	global_store_dwordx4 v[86:87], v[18:21], off sc1
	v_pk_add_f32 v[16:17], v[16:17], v[28:29]
	v_pk_add_f32 v[14:15], v[14:15], v[26:27]
	v_pk_add_f32 v[20:21], v[12:13], v[40:41]
	v_pk_add_f32 v[18:19], v[10:11], v[38:39]
	global_store_dwordx4 v[86:87], v[18:21], off offset:64 sc1
	v_pk_add_f32 v[12:13], v[12:13], v[24:25]
	v_pk_add_f32 v[10:11], v[10:11], v[22:23]
	v_pk_add_f32 v[20:21], v[8:9], v[52:53]
	v_pk_add_f32 v[18:19], v[6:7], v[50:51]
	global_store_dwordx4 v[86:87], v[18:21], off offset:512 sc1
	v_pk_add_f32 v[8:9], v[8:9], v[36:37]
	v_pk_add_f32 v[6:7], v[6:7], v[34:35]
	v_pk_add_f32 v[20:21], v[4:5], v[48:49]
	v_pk_add_f32 v[18:19], v[2:3], v[46:47]
	v_pk_add_f32 v[4:5], v[4:5], v[32:33]
	v_pk_add_f32 v[2:3], v[2:3], v[30:31]
	global_store_dwordx4 v[86:87], v[18:21], off offset:576 sc1
	global_store_dwordx4 v[0:1], v[14:17], off sc1
	global_store_dwordx4 v[0:1], v[10:13], off offset:64 sc1
	global_store_dwordx4 v[0:1], v[6:9], off offset:512 sc1
	global_store_dwordx4 v[0:1], v[2:5], off offset:576 sc1
	s_waitcnt vmcnt(0)
	s_cbranch_scc1 .LBB2_6
	s_barrier

	.amdhsa_kernel _Z11out2_kernelPKtS0_PfPKf
		.amdhsa_group_segment_fixed_size 0
		.amdhsa_private_segment_fixed_size 0
		.amdhsa_kernarg_size 32
		.amdhsa_user_sgpr_count 2
		.amdhsa_user_sgpr_dispatch_ptr 0
		.amdhsa_user_sgpr_queue_ptr 0
		.amdhsa_user_sgpr_kernarg_segment_ptr 1
		.amdhsa_user_sgpr_dispatch_id 0
		.amdhsa_user_sgpr_kernarg_preload_length 0
		.amdhsa_user_sgpr_kernarg_preload_offset 0
		.amdhsa_user_sgpr_private_segment_size 0
		.amdhsa_uses_dynamic_stack 0
		.amdhsa_enable_private_segment 0
		.amdhsa_system_sgpr_workgroup_id_x 1
		.amdhsa_system_sgpr_workgroup_id_y 0
		.amdhsa_system_sgpr_workgroup_id_z 0
		.amdhsa_system_sgpr_workgroup_info 0
		.amdhsa_system_vgpr_workitem_id 0
		.amdhsa_next_free_vgpr 160
		.amdhsa_next_free_sgpr 22
		.amdhsa_accum_offset 160
		.amdhsa_reserve_vcc 0
		.amdhsa_float_round_mode_32 0
		.amdhsa_float_round_mode_16_64 0
		.amdhsa_float_denorm_mode_32 3
		.amdhsa_float_denorm_mode_16_64 3
		.amdhsa_dx10_clamp 1
		.amdhsa_ieee_mode 1
		.amdhsa_fp16_overflow 0
		.amdhsa_tg_split 0
		.amdhsa_exception_fp_ieee_invalid_op 0
		.amdhsa_exception_fp_denorm_src 0
		.amdhsa_exception_fp_ieee_div_zero 0
		.amdhsa_exception_fp_ieee_overflow 0
		.amdhsa_exception_fp_ieee_underflow 0
		.amdhsa_exception_fp_ieee_inexact 0
		.amdhsa_exception_int_div_zero 0
	.end_amdhsa_kernel

amdhsa.kernels:
  - .agpr_count:     0
    .args:
      - .actual_access:  read_only
        .address_space:  global
        .offset:         0
        .size:           8
        .value_kind:     global_buffer
      - .actual_access:  read_only
        .address_space:  global
        .offset:         8
        .size:           8
        .value_kind:     global_buffer
      - .actual_access:  read_only
        .address_space:  global
        .offset:         16
        .size:           8
        .value_kind:     global_buffer
      - .actual_access:  write_only
        .address_space:  global
        .offset:         24
        .size:           8
        .value_kind:     global_buffer
      - .actual_access:  write_only
        .address_space:  global
        .offset:         32
        .size:           8
        .value_kind:     global_buffer
      - .actual_access:  write_only
        .address_space:  global
        .offset:         40
        .size:           8
        .value_kind:     global_buffer
    .group_segment_fixed_size: 0
    .kernarg_segment_align: 8
    .kernarg_segment_size: 48
    .language:       OpenCL C
    .language_version:
      - 2
      - 0
    .max_flat_workgroup_size: 256
    .name:           _Z10cvt_kernelPKfS0_S0_PtS1_S1_
    .private_segment_fixed_size: 0
    .sgpr_count:     16
    .sgpr_spill_count: 0
    .symbol:         _Z10cvt_kernelPKfS0_S0_PtS1_S1_.kd
    .uniform_work_group_size: 1
    .uses_dynamic_stack: false
    .vgpr_count:     40
    .vgpr_spill_count: 0
    .wavefront_size: 64
  - .agpr_count:     0
    .args:
      - .address_space:  global
        .offset:         0
        .size:           8
        .value_kind:     global_buffer
      - .address_space:  global
        .offset:         8
        .size:           8
        .value_kind:     global_buffer
      - .address_space:  global
        .offset:         16
        .size:           8
        .value_kind:     global_buffer
      - .address_space:  global
        .offset:         24
        .size:           8
        .value_kind:     global_buffer
      - .address_space:  global
        .offset:         32
        .size:           8
        .value_kind:     global_buffer
      - .address_space:  global
        .offset:         40
        .size:           8
        .value_kind:     global_buffer
    .group_segment_fixed_size: 0
    .kernarg_segment_align: 8
    .kernarg_segment_size: 48
    .language:       OpenCL C
    .language_version:
      - 2
      - 0
    .max_flat_workgroup_size: 512
    .name:           _Z10kvq_kernelPKtS0_PtS1_S1_PKf
    .private_segment_fixed_size: 0
    .sgpr_count:     44
    .sgpr_spill_count: 0
    .symbol:         _Z10kvq_kernelPKtS0_PtS1_S1_PKf.kd
    .uniform_work_group_size: 1
    .uses_dynamic_stack: false
    .vgpr_count:     176
    .vgpr_spill_count: 0
    .wavefront_size: 64
  - .agpr_count:     0
    .args:
      - .address_space:  global
        .offset:         0
        .size:           8
        .value_kind:     global_buffer
      - .address_space:  global
        .offset:         8
        .size:           8
        .value_kind:     global_buffer
      - .address_space:  global
        .offset:         16
        .size:           8
        .value_kind:     global_buffer
      - .address_space:  global
        .offset:         24
        .size:           8
        .value_kind:     global_buffer
    .group_segment_fixed_size: 0
    .kernarg_segment_align: 8
    .kernarg_segment_size: 32
    .language:       OpenCL C
    .language_version:
      - 2
      - 0
    .max_flat_workgroup_size: 512
    .name:           _Z11out2_kernelPKtS0_PfPKf
    .private_segment_fixed_size: 0
    .sgpr_count:     28
    .sgpr_spill_count: 0
    .symbol:         _Z11out2_kernelPKtS0_PfPKf.kd
    .uniform_work_group_size: 1
    .uses_dynamic_stack: false
    .vgpr_count:     160
    .vgpr_spill_count: 0
    .wavefront_size: 64
  - .agpr_count:     0
    .args:
      - .address_space:  global
        .offset:         0
        .size:           8
        .value_kind:     global_buffer
      - .address_space:  global
        .offset:         8
        .size:           8
        .value_kind:     global_buffer
      - .address_space:  global
        .offset:         16
        .size:           8
        .value_kind:     global_buffer
      - .address_space:  global
        .offset:         24
        .size:           8
        .value_kind:     global_buffer
      - .offset:         32
        .size:           4
        .value_kind:     hidden_block_count_x
      - .offset:         36
        .size:           4
        .value_kind:     hidden_block_count_y
      - .offset:         40
        .size:           4
        .value_kind:     hidden_block_count_z
      - .offset:         44
        .size:           2
        .value_kind:     hidden_group_size_x
      - .offset:         46
        .size:           2
        .value_kind:     hidden_group_size_y
      - .offset:         48
        .size:           2
        .value_kind:     hidden_group_size_z
      - .offset:         50
        .size:           2
        .value_kind:     hidden_remainder_x
      - .offset:         52
        .size:           2
        .value_kind:     hidden_remainder_y
      - .offset:         54
        .size:           2
        .value_kind:     hidden_remainder_z
      - .offset:         72
        .size:           8
        .value_kind:     hidden_global_offset_x
      - .offset:         80
        .size:           8
        .value_kind:     hidden_global_offset_y
      - .offset:         88
        .size:           8
        .value_kind:     hidden_global_offset_z
      - .offset:         96
        .size:           2
        .value_kind:     hidden_grid_dims
      - .offset:         152
        .size:           4
        .value_kind:     hidden_dynamic_lds_size
    .group_segment_fixed_size: 0
    .kernarg_segment_align: 8
    .kernarg_segment_size: 288
    .language:       OpenCL C
    .language_version:
      - 2
      - 0
    .max_flat_workgroup_size: 512
    .name:           _Z11attn_kernelPKtS0_S0_Pt
    .private_segment_fixed_size: 0
    .sgpr_count:     53
    .sgpr_spill_count: 0
    .symbol:         _Z11attn_kernelPKtS0_S0_Pt.kd
    .uniform_work_group_size: 1
    .uses_dynamic_stack: false
    .vgpr_count:     256
    .vgpr_spill_count: 0
    .wavefront_size: 64
